# v048 + P13 tile loop edge straightened + P3 early-exit ballot trimmed (exact edits only)
# baseline (speedup 1.0000x reference)
.LBB0_2756:
	s_barrier
	ds_read_b64 v[226:227], v146
	s_lshl_b32 s39, s37, 14
	s_cmp_le_u32 s38, s34
	s_cbranch_scc0 .LBB0_2751
	s_add_i32 s14, s39, 0xffffc000
	s_cmp_lg_u32 s37, 0
	s_cselect_b32 s40, s14, 0x8000
	v_lshl_add_u64 v[82:83], v[182:183], 0, s[0:1]
	s_mov_b64 s[14:15], 0x39208000
	s_add_i32 s40, s22, s40
	v_lshl_add_u64 v[84:85], v[82:83], 0, s[14:15]
	s_mov_b32 m0, s40
	s_mov_b64 s[14:15], 0x39208080
	global_load_lds_dwordx4 v[84:85], off
	v_lshl_add_u64 v[82:83], v[82:83], 0, s[14:15]
	s_add_i32 m0, s40, 0x2000
	s_mov_b64 s[14:15], 0x3a208000
	global_load_lds_dwordx4 v[82:83], off
	v_lshl_add_u64 v[82:83], v[172:173], 0, s[0:1]
	v_lshl_add_u64 v[84:85], v[82:83], 0, s[14:15]
	s_add_i32 m0, s40, 0xc000
	v_lshl_add_u64 v[82:83], v[82:83], 0, s[12:13]
	global_load_lds_dwordx4 v[84:85], off
	s_add_i32 m0, s40, 0xe000
	s_nop 0
	global_load_lds_dwordx4 v[82:83], off
	s_branch .LBB0_2751
